# code prefetch of the next phase issued by waves 1-7 (after a short sleep, so that it follows the leader wave's acquire) while the workgroup waits in each grid barrier; replaces the phase-entry prefetc
# baseline (speedup 1.0000x reference)
.LBB0_81:
	s_or_b64 exec, exec, s[0:1]
	s_cmp_gt_i32 s89, 1
	s_cbranch_scc0 .LBB0_135
	s_waitcnt vmcnt(0)
	s_barrier
	v_cmp_lt_u32_e32 vcc, 63, v0
	s_and_saveexec_b64 s[4:5], vcc
	s_cbranch_execz .Lbw_skip_0
	s_sleep 80
	s_getpc_b64 s[10:11]
	s_and_b32 s10, s10, 0xffffff80
	v_readlane_b32 s97, v252, 2
	s_nop 0
	s_and_b32 s97, s97, 31
	s_mul_i32 s97, s97, 0x180
	s_add_u32 s10, s10, s97
	s_addc_u32 s11, s11, 0
	v_and_b32_e32 v254, 63, v0
	v_min_u32_e32 v254, 2, v254
	v_lshlrev_b32_e32 v254, 7, v254
	global_load_dword v254, v254, s[10:11]
.Lbw_skip_0:
	s_or_b64 exec, exec, s[4:5]
	s_and_saveexec_b64 s[0:1], s[94:95]
	s_cbranch_execz .LBB0_134
	s_add_i32 s4, 0, 0x26d60
	v_mov_b32_e32 v1, s4
	s_waitcnt vmcnt(0) expcnt(0) lgkmcnt(0)
	ds_read_b32 v3, v1
	s_add_i32 s4, 0, 0x26d64
	v_mov_b32_e32 v1, s4
	ds_read_b32 v1, v1
	s_waitcnt lgkmcnt(1)
	v_cmp_ne_u32_e32 vcc, 0, v3
	s_cbranch_vccnz .LBB0_98
	v_readlane_b32 s4, v252, 0
	v_readlane_b32 s5, v252, 1
	s_load_dwordx2 s[12:13], s[4:5], 0x4
	s_add_u32 s4, s86, 0x1000
	s_addc_u32 s5, s87, 0
	s_add_u32 s10, s86, 0x1100
	s_addc_u32 s11, s87, 0
	s_waitcnt lgkmcnt(0)
	s_mul_i32 s22, s12, s84
	s_add_u32 s12, s86, 0x1200
	s_mul_i32 s22, s22, s13
	s_addc_u32 s13, s87, 0
	s_add_u32 s14, s86, 0x1300
	s_addc_u32 s15, s87, 0
	s_mov_b32 s23, 1
	v_mov_b32_e32 v17, 0
	s_branch .LBB0_86

.LBB0_160:
	s_cmp_lt_i32 s89, 3
	s_cbranch_scc1 .LBB0_214
	s_waitcnt vmcnt(0)
	s_waitcnt vmcnt(0)
	s_barrier
	v_cmp_lt_u32_e32 vcc, 63, v0
	s_and_saveexec_b64 s[4:5], vcc
	s_cbranch_execz .Lbw_skip_1
	s_sleep 80
	s_getpc_b64 s[10:11]
	s_and_b32 s10, s10, 0xffffff80
	v_readlane_b32 s97, v252, 2
	s_nop 0
	s_and_b32 s97, s97, 31
	s_mul_i32 s97, s97, 0x480
	s_add_u32 s10, s10, s97
	s_addc_u32 s11, s11, 0
	v_and_b32_e32 v254, 63, v0
	v_min_u32_e32 v254, 8, v254
	v_lshlrev_b32_e32 v254, 7, v254
	global_load_dword v254, v254, s[10:11]

.LBB0_473:
.LBB0_479:
	s_cmp_gt_i32 s89, 3
	s_cbranch_scc0 .LBB0_533
	s_waitcnt vmcnt(0)
	s_waitcnt vmcnt(0)
	s_barrier
	v_cmp_lt_u32_e32 vcc, 63, v0
	s_and_saveexec_b64 s[4:5], vcc
	s_cbranch_execz .Lbw_skip_2
	s_sleep 80
	s_getpc_b64 s[10:11]
	s_and_b32 s10, s10, 0xffffff80
	v_readlane_b32 s97, v252, 2
	s_nop 0
	s_and_b32 s97, s97, 31
	s_mul_i32 s97, s97, 0x480
	s_add_u32 s10, s10, s97
	s_addc_u32 s11, s11, 0
	v_and_b32_e32 v254, 63, v0
	v_min_u32_e32 v254, 8, v254
	v_lshlrev_b32_e32 v254, 7, v254
	global_load_dword v254, v254, s[10:11]

.LBB0_1240:
	s_cmp_lt_i32 s89, 5
	s_cbranch_scc1 .LBB0_1294
	s_waitcnt vmcnt(0)
	s_waitcnt vmcnt(63) expcnt(7) lgkmcnt(15)
	s_barrier
	v_cmp_lt_u32_e32 vcc, 63, v0
	s_and_saveexec_b64 s[4:5], vcc
	s_cbranch_execz .Lbw_skip_3
	s_sleep 80
	s_getpc_b64 s[10:11]
	s_and_b32 s10, s10, 0xffffff80
	v_readlane_b32 s97, v252, 2
	s_nop 0
	s_and_b32 s97, s97, 31
	s_mul_i32 s97, s97, 0x300
	s_add_u32 s10, s10, s97
	s_addc_u32 s11, s11, 0
	v_and_b32_e32 v254, 63, v0
	v_min_u32_e32 v254, 5, v254
	v_lshlrev_b32_e32 v254, 7, v254
	global_load_dword v254, v254, s[10:11]
.Lbw_skip_3:
	s_or_b64 exec, exec, s[4:5]
	s_and_saveexec_b64 s[0:1], s[94:95]
	s_cbranch_execz .LBB0_1293
	s_add_i32 s3, 0, 0x26d60
	v_mov_b32_e32 v1, s3
	s_waitcnt vmcnt(0) expcnt(0) lgkmcnt(0)
	ds_read_b32 v3, v1
	s_add_i32 s3, 0, 0x26d64
	v_mov_b32_e32 v1, s3
	ds_read_b32 v1, v1
	s_waitcnt lgkmcnt(1)
	v_cmp_ne_u32_e32 vcc, 0, v3
	s_cbranch_vccnz .LBB0_1257
	v_readlane_b32 s4, v252, 0
	v_readlane_b32 s5, v252, 1
	s_load_dwordx2 s[8:9], s[4:5], 0x4
	s_add_u32 s4, s86, 0x1000
	s_addc_u32 s5, s87, 0
	s_add_u32 s6, s86, 0x1100
	s_addc_u32 s7, s87, 0
	s_waitcnt lgkmcnt(0)
	s_mul_i32 s3, s8, s84
	s_add_u32 s8, s86, 0x1200
	s_mul_i32 s3, s3, s9
	s_addc_u32 s9, s87, 0
	s_add_u32 s10, s86, 0x1300
	s_addc_u32 s11, s87, 0
	s_mov_b32 s18, 1
	v_mov_b32_e32 v17, 0
	s_branch .LBB0_1245

.LBB0_1373:
	s_cmp_gt_i32 s89, 5
	s_cbranch_scc0 .LBB0_1427
	s_waitcnt vmcnt(0)
	s_waitcnt vmcnt(0)
	s_barrier
	v_cmp_lt_u32_e32 vcc, 63, v0
	s_and_saveexec_b64 s[4:5], vcc
	s_cbranch_execz .Lbw_skip_4
	s_sleep 80
	s_getpc_b64 s[10:11]
	s_and_b32 s10, s10, 0xffffff80
	v_readlane_b32 s97, v252, 2
	s_nop 0
	s_and_b32 s97, s97, 31
	s_mul_i32 s97, s97, 0x200
	s_add_u32 s10, s10, s97
	s_addc_u32 s11, s11, 0
	v_and_b32_e32 v254, 63, v0
	v_min_u32_e32 v254, 3, v254
	v_lshlrev_b32_e32 v254, 7, v254
	global_load_dword v254, v254, s[10:11]
